# speedup vs baseline: 1.0077x; 1.0035x over previous
.Lep1_prej:
	s_waitcnt lgkmcnt(7)
	s_barrier
	s_cmp_eq_u64 s[6:7], 0
	s_cbranch_scc0 .Lep1_k1
	s_mul_i32 s43, s36, 0x5000
	s_add_i32 s43, s43, s86
	s_add_u32 s40, s18, s43
	s_addc_u32 s41, s19, 0
	v_mov_b32_e32 v18, 0
	v_mov_b32_e32 v19, 0
	v_mov_b32_e32 v20, 0
	v_mov_b32_e32 v21, 0
	ds_read2st64_b32 v[50:51], v221 offset0:0 offset1:1
	ds_read2st64_b32 v[52:53], v221 offset0:2 offset1:3
	ds_read2st64_b32 v[54:55], v221 offset0:4 offset1:5
	ds_read2st64_b32 v[56:57], v221 offset0:6 offset1:7
	ds_read2st64_b32 v[58:59], v221 offset0:8 offset1:9
	ds_read2st64_b32 v[60:61], v221 offset0:10 offset1:11
	s_waitcnt lgkmcnt(12)
	v_fma_f32 v78, -v76, v77, 0
	s_waitcnt lgkmcnt(4)
	v_pk_add_f32 v[34:35], v[34:35], v[50:51]
	v_pk_add_f32 v[36:37], v[36:37], v[52:53]
	v_pk_add_f32 v[34:35], v[34:35], v[78:79] op_sel_hi:[1,0]
	v_pk_add_f32 v[36:37], v[36:37], v[78:79] op_sel_hi:[1,0]
	v_pk_fma_f32 v[34:35], v[62:63], v[76:77], v[34:35] op_sel:[0,1,0] op_sel_hi:[1,1,1]
	v_pk_fma_f32 v[36:37], v[64:65], v[76:77], v[36:37] op_sel:[0,1,0] op_sel_hi:[1,1,1]
	v_pk_add_f32 v[18:19], v[18:19], v[34:35]
	v_pk_fma_f32 v[20:21], v[34:35], v[34:35], v[20:21]
	v_pk_add_f32 v[18:19], v[18:19], v[36:37]
	v_pk_fma_f32 v[20:21], v[36:37], v[36:37], v[20:21]
	s_waitcnt lgkmcnt(2)
	v_pk_add_f32 v[38:39], v[38:39], v[54:55]
	v_pk_add_f32 v[40:41], v[40:41], v[56:57]
	v_pk_add_f32 v[38:39], v[38:39], v[78:79] op_sel_hi:[1,0]
	v_pk_add_f32 v[40:41], v[40:41], v[78:79] op_sel_hi:[1,0]
	v_pk_fma_f32 v[38:39], v[68:69], v[76:77], v[38:39] op_sel:[0,1,0] op_sel_hi:[1,1,1]
	v_pk_fma_f32 v[40:41], v[70:71], v[76:77], v[40:41] op_sel:[0,1,0] op_sel_hi:[1,1,1]
	v_pk_add_f32 v[18:19], v[18:19], v[38:39]
	v_pk_fma_f32 v[20:21], v[38:39], v[38:39], v[20:21]
	v_pk_add_f32 v[18:19], v[18:19], v[40:41]
	v_pk_fma_f32 v[20:21], v[40:41], v[40:41], v[20:21]
	s_waitcnt lgkmcnt(0)
	v_pk_add_f32 v[42:43], v[42:43], v[58:59]
	v_pk_add_f32 v[44:45], v[44:45], v[60:61]
	v_pk_add_f32 v[42:43], v[42:43], v[78:79] op_sel_hi:[1,0]
	v_pk_add_f32 v[44:45], v[44:45], v[78:79] op_sel_hi:[1,0]
	v_pk_fma_f32 v[42:43], v[72:73], v[76:77], v[42:43] op_sel:[0,1,0] op_sel_hi:[1,1,1]
	v_pk_fma_f32 v[44:45], v[74:75], v[76:77], v[44:45] op_sel:[0,1,0] op_sel_hi:[1,1,1]
	v_pk_add_f32 v[18:19], v[18:19], v[42:43]
	v_pk_fma_f32 v[20:21], v[42:43], v[42:43], v[20:21]
	v_pk_add_f32 v[18:19], v[18:19], v[44:45]
	v_pk_fma_f32 v[20:21], v[44:45], v[44:45], v[20:21]
	ds_read2st64_b32 v[50:51], v221 offset0:12 offset1:13
	ds_read2st64_b32 v[52:53], v221 offset0:14 offset1:15
	ds_read2st64_b32 v[54:55], v221 offset0:16 offset1:17
	ds_read2st64_b32 v[56:57], v221 offset0:18 offset1:19
	ds_read2st64_b32 v[58:59], v221 offset0:20 offset1:21
	ds_read2st64_b32 v[60:61], v221 offset0:22 offset1:23
	ds_read2st64_b32 v[62:63], v67 offset0:48 offset1:50
	ds_read2st64_b32 v[64:65], v67 offset0:52 offset1:54
	ds_read2st64_b32 v[68:69], v67 offset0:64 offset1:66
	ds_read2st64_b32 v[70:71], v67 offset0:68 offset1:70
	ds_read2st64_b32 v[72:73], v67 offset0:80 offset1:82
	ds_read2st64_b32 v[74:75], v67 offset0:84 offset1:86
	s_barrier
	ds_read_b32 v80, v236
	s_waitcnt lgkmcnt(5)
	v_pk_add_f32 v[46:47], v[46:47], v[50:51]
	v_pk_add_f32 v[48:49], v[48:49], v[52:53]
	v_pk_add_f32 v[46:47], v[46:47], v[78:79] op_sel_hi:[1,0]
	v_pk_add_f32 v[48:49], v[48:49], v[78:79] op_sel_hi:[1,0]
	v_pk_fma_f32 v[46:47], v[62:63], v[76:77], v[46:47] op_sel:[0,1,0] op_sel_hi:[1,1,1]
	v_pk_fma_f32 v[48:49], v[64:65], v[76:77], v[48:49] op_sel:[0,1,0] op_sel_hi:[1,1,1]
	v_pk_add_f32 v[18:19], v[18:19], v[46:47]
	v_pk_fma_f32 v[20:21], v[46:47], v[46:47], v[20:21]
	v_pk_add_f32 v[18:19], v[18:19], v[48:49]
	v_pk_fma_f32 v[20:21], v[48:49], v[48:49], v[20:21]
	s_waitcnt lgkmcnt(3)
	v_pk_add_f32 v[2:3], v[2:3], v[54:55]
	v_pk_add_f32 v[4:5], v[4:5], v[56:57]
	v_pk_add_f32 v[2:3], v[2:3], v[78:79] op_sel_hi:[1,0]
	v_pk_add_f32 v[4:5], v[4:5], v[78:79] op_sel_hi:[1,0]
	v_pk_fma_f32 v[2:3], v[68:69], v[76:77], v[2:3] op_sel:[0,1,0] op_sel_hi:[1,1,1]
	v_pk_fma_f32 v[4:5], v[70:71], v[76:77], v[4:5] op_sel:[0,1,0] op_sel_hi:[1,1,1]
	v_pk_add_f32 v[18:19], v[18:19], v[2:3]
	v_pk_fma_f32 v[20:21], v[2:3], v[2:3], v[20:21]
	v_pk_add_f32 v[18:19], v[18:19], v[4:5]
	v_pk_fma_f32 v[20:21], v[4:5], v[4:5], v[20:21]
	s_waitcnt lgkmcnt(1)
	v_pk_add_f32 v[6:7], v[6:7], v[58:59]
	v_pk_add_f32 v[8:9], v[8:9], v[60:61]
	v_pk_add_f32 v[6:7], v[6:7], v[78:79] op_sel_hi:[1,0]
	v_pk_add_f32 v[8:9], v[8:9], v[78:79] op_sel_hi:[1,0]
	v_pk_fma_f32 v[6:7], v[72:73], v[76:77], v[6:7] op_sel:[0,1,0] op_sel_hi:[1,1,1]
	v_pk_fma_f32 v[8:9], v[74:75], v[76:77], v[8:9] op_sel:[0,1,0] op_sel_hi:[1,1,1]
	v_pk_add_f32 v[18:19], v[18:19], v[6:7]
	v_pk_fma_f32 v[20:21], v[6:7], v[6:7], v[20:21]
	v_pk_add_f32 v[18:19], v[18:19], v[8:9]
	v_pk_fma_f32 v[20:21], v[8:9], v[8:9], v[20:21]
	v_add_f32_e32 v18, v18, v19
	v_add_f32_e32 v20, v20, v21
	s_nop 1
	v_permlane32_swap_b32_e32 v18, v20
	v_add_f32_e32 v22, v18, v20
	s_branch .Lep1_wr0

.Lep1_wr0:
	s_waitcnt lgkmcnt(0)
	v_add_f32_e32 v22, v22, v80
	s_mov_b32 exec_hi, 0xfffffff
	v_cndmask_b32_e64 v57, v22, 1.0, s[84:85]
	v_writelane_b32 v22, 1.0, 0
	global_atomic_add_f32 v253, v57, s[40:41]
	s_mov_b32 exec_lo, 0xf0000001
	s_mov_b32 exec_hi, 0xf0000000
	global_atomic_add_f32 v254, v22, s[40:41]
	s_mov_b64 exec, -1
	ds_write2st64_b32 v67, v34, v35 offset0:0 offset1:2
	ds_write2st64_b32 v67, v36, v37 offset0:4 offset1:6
	ds_write2st64_b32 v67, v38, v39 offset0:16 offset1:18
	ds_write2st64_b32 v67, v40, v41 offset0:20 offset1:22
	ds_write2st64_b32 v67, v42, v43 offset0:32 offset1:34
	ds_write2st64_b32 v67, v44, v45 offset0:36 offset1:38
	ds_write2st64_b32 v67, v46, v47 offset0:48 offset1:50
	ds_write2st64_b32 v67, v48, v49 offset0:52 offset1:54
	ds_write2st64_b32 v67, v2, v3 offset0:64 offset1:66
	ds_write2st64_b32 v67, v4, v5 offset0:68 offset1:70
	ds_write2st64_b32 v67, v6, v7 offset0:80 offset1:82
	ds_write2st64_b32 v67, v8, v9 offset0:84 offset1:86
	s_branch .Lep1_end

.LBB1_126:
	s_or_b64 exec, exec, s[30:31]
	v_mov_b32_e32 v132, v0
	s_waitcnt lgkmcnt(0)
	s_barrier
	s_lshl_b64 s[2:3], s[36:37], 16
	v_and_b32_e32 v134, 31, v132
	v_lshlrev_b32_e32 v58, 4, v134
	v_add_u32_e32 v59, 0x25680, v58
	v_add_u32_e32 v58, 0x25880, v58
	ds_read_b128 v[62:65], v59
	ds_read_b128 v[58:61], v58
	v_ashrrev_i32_e32 v133, 5, v132
	v_lshlrev_b32_e32 v132, 3, v134
	v_mad_u32_u24 v134, v133, s64, v132
	s_waitcnt lgkmcnt(0)
	v_pk_mul_f32 v[62:63], v[62:63], v[58:59] neg_lo:[1,0] neg_hi:[1,0]
	v_pk_mul_f32 v[64:65], v[64:65], v[60:61] neg_lo:[1,0] neg_hi:[1,0]
	v_pk_fma_f32 v[54:55], v[54:55], v[58:59], v[62:63]
	v_pk_fma_f32 v[56:57], v[56:57], v[60:61], v[64:65]
	v_pk_fma_f32 v[50:51], v[50:51], v[58:59], v[62:63]
	v_pk_fma_f32 v[52:53], v[52:53], v[60:61], v[64:65]
	v_pk_fma_f32 v[46:47], v[46:47], v[58:59], v[62:63]
	v_pk_fma_f32 v[48:49], v[48:49], v[60:61], v[64:65]
	v_pk_fma_f32 v[42:43], v[42:43], v[58:59], v[62:63]
	v_pk_fma_f32 v[44:45], v[44:45], v[60:61], v[64:65]
	v_pk_fma_f32 v[38:39], v[38:39], v[58:59], v[62:63]
	v_pk_fma_f32 v[40:41], v[40:41], v[60:61], v[64:65]
	v_cvt_pk_f16_f32 v54, v54, v55
	v_cvt_pk_f16_f32 v55, v56, v57
	ds_write_b64 v134, v[54:55] offset:43008
	v_cvt_pk_f16_f32 v50, v50, v51
	v_cvt_pk_f16_f32 v51, v52, v53
	ds_write_b64 v134, v[50:51] offset:47360
	v_cvt_pk_f16_f32 v46, v46, v47
	v_cvt_pk_f16_f32 v47, v48, v49
	ds_write_b64 v134, v[46:47] offset:51712
	v_cvt_pk_f16_f32 v42, v42, v43
	v_cvt_pk_f16_f32 v43, v44, v45
	ds_write_b64 v134, v[42:43] offset:56064
	v_cvt_pk_f16_f32 v38, v38, v39
	v_cvt_pk_f16_f32 v39, v40, v41
	ds_write_b64 v134, v[38:39] offset:60416
	v_cmp_gt_i32_e32 vcc, 4, v133
	s_and_saveexec_b64 s[30:31], vcc
	v_pk_fma_f32 v[34:35], v[34:35], v[58:59], v[62:63]
	v_pk_fma_f32 v[36:37], v[36:37], v[60:61], v[64:65]
	v_cvt_pk_f16_f32 v34, v34, v35
	v_cvt_pk_f16_f32 v35, v36, v37
	ds_write_b64 v134, v[34:35] offset:64768
	s_or_b64 exec, exec, s[30:31]
	s_waitcnt lgkmcnt(0)
	s_barrier
	v_or_b32_e32 v34, s26, v220
	v_mov_b32_e32 v35, v66
	v_lshl_add_u64 v[34:35], v[34:35], 2, s[28:29]
	v_lshl_add_u64 v[174:175], s[2:3], 1, v[214:215]
	global_load_dword v173, v[34:35], off
	global_load_dwordx4 v[136:139], v[174:175], off
	global_load_dwordx4 v[132:135], v[174:175], off offset:1024
	v_add_u32_e32 v34, v204, v238
	ds_read_b128 v[168:171], v34 offset:43008
	ds_read_b128 v[164:167], v34 offset:43040
	ds_read_b128 v[160:163], v34 offset:43072
	ds_read_b128 v[156:159], v34 offset:43104
	ds_read_b128 v[152:155], v34 offset:43136
	ds_read_b128 v[148:151], v34 offset:43168
	ds_read_b128 v[144:147], v34 offset:43200
	ds_read_b128 v[140:143], v34 offset:43232
	s_mov_b32 s30, 0
	s_mov_b64 s[2:3], -1

.Lep2_prej:
	s_waitcnt lgkmcnt(7)
	s_barrier
	s_cmp_eq_u64 s[6:7], 0
	s_cbranch_scc0 .Lep2_k1
	s_mul_i32 s43, s36, 0x5000
	s_addk_i32 s43, 0x2800
	s_add_i32 s43, s43, s86
	s_add_u32 s40, s18, s43
	s_addc_u32 s41, s19, 0
	v_mov_b32_e32 v18, 0
	v_mov_b32_e32 v19, 0
	v_mov_b32_e32 v20, 0
	v_mov_b32_e32 v21, 0
	ds_read2st64_b32 v[50:51], v221 offset0:0 offset1:1
	ds_read2st64_b32 v[52:53], v221 offset0:2 offset1:3
	ds_read2st64_b32 v[54:55], v221 offset0:4 offset1:5
	ds_read2st64_b32 v[56:57], v221 offset0:6 offset1:7
	ds_read2st64_b32 v[58:59], v221 offset0:8 offset1:9
	ds_read2st64_b32 v[60:61], v221 offset0:10 offset1:11
	s_waitcnt lgkmcnt(12)
	v_fma_f32 v78, -v76, v77, v173
	s_waitcnt lgkmcnt(4)
	v_pk_add_f32 v[34:35], v[34:35], v[50:51]
	v_pk_add_f32 v[36:37], v[36:37], v[52:53]
	v_pk_add_f32 v[34:35], v[34:35], v[78:79] op_sel_hi:[1,0]
	v_pk_add_f32 v[36:37], v[36:37], v[78:79] op_sel_hi:[1,0]
	v_pk_fma_f32 v[34:35], v[62:63], v[76:77], v[34:35] op_sel:[0,1,0] op_sel_hi:[1,1,1]
	v_pk_fma_f32 v[36:37], v[64:65], v[76:77], v[36:37] op_sel:[0,1,0] op_sel_hi:[1,1,1]
	v_pk_add_f32 v[18:19], v[18:19], v[34:35]
	v_pk_fma_f32 v[20:21], v[34:35], v[34:35], v[20:21]
	v_pk_add_f32 v[18:19], v[18:19], v[36:37]
	v_pk_fma_f32 v[20:21], v[36:37], v[36:37], v[20:21]
	s_waitcnt lgkmcnt(2)
	v_pk_add_f32 v[38:39], v[38:39], v[54:55]
	v_pk_add_f32 v[40:41], v[40:41], v[56:57]
	v_pk_add_f32 v[38:39], v[38:39], v[78:79] op_sel_hi:[1,0]
	v_pk_add_f32 v[40:41], v[40:41], v[78:79] op_sel_hi:[1,0]
	v_pk_fma_f32 v[38:39], v[68:69], v[76:77], v[38:39] op_sel:[0,1,0] op_sel_hi:[1,1,1]
	v_pk_fma_f32 v[40:41], v[70:71], v[76:77], v[40:41] op_sel:[0,1,0] op_sel_hi:[1,1,1]
	v_pk_add_f32 v[18:19], v[18:19], v[38:39]
	v_pk_fma_f32 v[20:21], v[38:39], v[38:39], v[20:21]
	v_pk_add_f32 v[18:19], v[18:19], v[40:41]
	v_pk_fma_f32 v[20:21], v[40:41], v[40:41], v[20:21]
	s_waitcnt lgkmcnt(0)
	v_pk_add_f32 v[42:43], v[42:43], v[58:59]
	v_pk_add_f32 v[44:45], v[44:45], v[60:61]
	v_pk_add_f32 v[42:43], v[42:43], v[78:79] op_sel_hi:[1,0]
	v_pk_add_f32 v[44:45], v[44:45], v[78:79] op_sel_hi:[1,0]
	v_pk_fma_f32 v[42:43], v[72:73], v[76:77], v[42:43] op_sel:[0,1,0] op_sel_hi:[1,1,1]
	v_pk_fma_f32 v[44:45], v[74:75], v[76:77], v[44:45] op_sel:[0,1,0] op_sel_hi:[1,1,1]
	v_pk_add_f32 v[18:19], v[18:19], v[42:43]
	v_pk_fma_f32 v[20:21], v[42:43], v[42:43], v[20:21]
	v_pk_add_f32 v[18:19], v[18:19], v[44:45]
	v_pk_fma_f32 v[20:21], v[44:45], v[44:45], v[20:21]
	ds_read2st64_b32 v[50:51], v221 offset0:12 offset1:13
	ds_read2st64_b32 v[52:53], v221 offset0:14 offset1:15
	ds_read2st64_b32 v[54:55], v221 offset0:16 offset1:17
	ds_read2st64_b32 v[56:57], v221 offset0:18 offset1:19
	ds_read2st64_b32 v[58:59], v221 offset0:20 offset1:21
	ds_read2st64_b32 v[60:61], v221 offset0:22 offset1:23
	ds_read2st64_b32 v[62:63], v67 offset0:48 offset1:50
	ds_read2st64_b32 v[64:65], v67 offset0:52 offset1:54
	ds_read2st64_b32 v[68:69], v67 offset0:64 offset1:66
	ds_read2st64_b32 v[70:71], v67 offset0:68 offset1:70
	ds_read2st64_b32 v[72:73], v67 offset0:80 offset1:82
	ds_read2st64_b32 v[74:75], v67 offset0:84 offset1:86
	s_barrier
	ds_read_b32 v80, v236
	s_waitcnt lgkmcnt(5)
	v_pk_add_f32 v[46:47], v[46:47], v[50:51]
	v_pk_add_f32 v[48:49], v[48:49], v[52:53]
	v_pk_add_f32 v[46:47], v[46:47], v[78:79] op_sel_hi:[1,0]
	v_pk_add_f32 v[48:49], v[48:49], v[78:79] op_sel_hi:[1,0]
	v_pk_fma_f32 v[46:47], v[62:63], v[76:77], v[46:47] op_sel:[0,1,0] op_sel_hi:[1,1,1]
	v_pk_fma_f32 v[48:49], v[64:65], v[76:77], v[48:49] op_sel:[0,1,0] op_sel_hi:[1,1,1]
	v_pk_add_f32 v[18:19], v[18:19], v[46:47]
	v_pk_fma_f32 v[20:21], v[46:47], v[46:47], v[20:21]
	v_pk_add_f32 v[18:19], v[18:19], v[48:49]
	v_pk_fma_f32 v[20:21], v[48:49], v[48:49], v[20:21]
	s_waitcnt lgkmcnt(3)
	v_pk_add_f32 v[2:3], v[2:3], v[54:55]
	v_pk_add_f32 v[4:5], v[4:5], v[56:57]
	v_pk_add_f32 v[2:3], v[2:3], v[78:79] op_sel_hi:[1,0]
	v_pk_add_f32 v[4:5], v[4:5], v[78:79] op_sel_hi:[1,0]
	v_pk_fma_f32 v[2:3], v[68:69], v[76:77], v[2:3] op_sel:[0,1,0] op_sel_hi:[1,1,1]
	v_pk_fma_f32 v[4:5], v[70:71], v[76:77], v[4:5] op_sel:[0,1,0] op_sel_hi:[1,1,1]
	v_pk_add_f32 v[18:19], v[18:19], v[2:3]
	v_pk_fma_f32 v[20:21], v[2:3], v[2:3], v[20:21]
	v_pk_add_f32 v[18:19], v[18:19], v[4:5]
	v_pk_fma_f32 v[20:21], v[4:5], v[4:5], v[20:21]
	s_waitcnt lgkmcnt(1)
	v_pk_add_f32 v[6:7], v[6:7], v[58:59]
	v_pk_add_f32 v[8:9], v[8:9], v[60:61]
	v_pk_add_f32 v[6:7], v[6:7], v[78:79] op_sel_hi:[1,0]
	v_pk_add_f32 v[8:9], v[8:9], v[78:79] op_sel_hi:[1,0]
	v_pk_fma_f32 v[6:7], v[72:73], v[76:77], v[6:7] op_sel:[0,1,0] op_sel_hi:[1,1,1]
	v_pk_fma_f32 v[8:9], v[74:75], v[76:77], v[8:9] op_sel:[0,1,0] op_sel_hi:[1,1,1]
	v_pk_add_f32 v[18:19], v[18:19], v[6:7]
	v_pk_fma_f32 v[20:21], v[6:7], v[6:7], v[20:21]
	v_pk_add_f32 v[18:19], v[18:19], v[8:9]
	v_pk_fma_f32 v[20:21], v[8:9], v[8:9], v[20:21]
	v_add_f32_e32 v18, v18, v19
	v_add_f32_e32 v20, v20, v21
	s_nop 1
	v_permlane32_swap_b32_e32 v18, v20
	v_add_f32_e32 v22, v18, v20
	s_branch .Lep2_wr0

.LBB1_207:
	s_or_b64 exec, exec, s[40:41]
	s_andn2_b64 vcc, exec, s[30:31]
	s_mov_b64 s[2:3], -1
	s_waitcnt lgkmcnt(0)
	s_barrier
	s_cbranch_vccnz .LBB1_221
	v_mov_b32_e32 v54, v0
	s_nop 0
	v_and_b32_e32 v56, 31, v54
	v_lshlrev_b32_e32 v46, 4, v56
	v_add_u32_e32 v47, 0x25680, v46
	v_add_u32_e32 v46, 0x25880, v46
	ds_read_b128 v[50:53], v47
	ds_read_b128 v[46:49], v46
	v_ashrrev_i32_e32 v55, 5, v54
	v_lshlrev_b32_e32 v54, 3, v56
	v_mad_u32_u24 v56, v55, s64, v54
	s_waitcnt lgkmcnt(0)
	v_pk_mul_f32 v[50:51], v[50:51], v[46:47] neg_lo:[1,0] neg_hi:[1,0]
	v_pk_mul_f32 v[52:53], v[52:53], v[48:49] neg_lo:[1,0] neg_hi:[1,0]
	v_pk_fma_f32 v[42:43], v[42:43], v[46:47], v[50:51]
	v_pk_fma_f32 v[44:45], v[44:45], v[48:49], v[52:53]
	v_pk_fma_f32 v[38:39], v[38:39], v[46:47], v[50:51]
	v_pk_fma_f32 v[40:41], v[40:41], v[48:49], v[52:53]
	v_pk_fma_f32 v[34:35], v[34:35], v[46:47], v[50:51]
	v_pk_fma_f32 v[36:37], v[36:37], v[48:49], v[52:53]
	v_pk_fma_f32 v[30:31], v[30:31], v[46:47], v[50:51]
	v_pk_fma_f32 v[32:33], v[32:33], v[48:49], v[52:53]
	v_pk_fma_f32 v[22:23], v[22:23], v[46:47], v[50:51]
	v_pk_fma_f32 v[24:25], v[24:25], v[48:49], v[52:53]
	v_cvt_pk_f16_f32 v42, v42, v43
	v_cvt_pk_f16_f32 v43, v44, v45
	ds_write_b64 v56, v[42:43] offset:43008
	v_cvt_pk_f16_f32 v38, v38, v39
	v_cvt_pk_f16_f32 v39, v40, v41
	ds_write_b64 v56, v[38:39] offset:47360
	v_cvt_pk_f16_f32 v34, v34, v35
	v_cvt_pk_f16_f32 v35, v36, v37
	ds_write_b64 v56, v[34:35] offset:51712
	v_cvt_pk_f16_f32 v30, v30, v31
	v_cvt_pk_f16_f32 v31, v32, v33
	ds_write_b64 v56, v[30:31] offset:56064
	v_cvt_pk_f16_f32 v22, v22, v23
	v_cvt_pk_f16_f32 v23, v24, v25
	ds_write_b64 v56, v[22:23] offset:60416
	v_cmp_gt_i32_e32 vcc, 4, v55
	s_and_saveexec_b64 s[2:3], vcc
	v_pk_fma_f32 v[18:19], v[18:19], v[46:47], v[50:51]
	v_pk_fma_f32 v[20:21], v[20:21], v[48:49], v[52:53]
	v_cvt_pk_f16_f32 v18, v18, v19
	v_cvt_pk_f16_f32 v19, v20, v21
	ds_write_b64 v56, v[18:19] offset:64768
	s_or_b64 exec, exec, s[2:3]
	s_mov_b64 s[2:3], 0
	s_waitcnt lgkmcnt(0)
	s_barrier
